# baseline (speedup 1.0000x reference)
.LBB0_19:
	s_cmp_lt_i32 s98, s82
	s_cbranch_scc0 .LBB0_35

.LBB0_30:
	s_add_i32 s6, s97, 0x2000
	s_cmpk_lg_i32 s97, 0x4000
	s_cselect_b32 s77, s6, 0
	s_setprio 1
	s_waitcnt lgkmcnt(14)
	v_mfma_f32_32x32x16_f16 v[50:65], v[194:197], v[158:161], v[50:65]
	v_exp_f32_e32 v98, v98
	v_exp_f32_e32 v99, v99
	v_exp_f32_e32 v100, v100
	v_exp_f32_e32 v101, v101
	s_waitcnt lgkmcnt(12)
	v_mfma_f32_32x32x16_f16 v[66:81], v[190:193], v[158:161], v[66:81]
	v_exp_f32_e32 v102, v102
	v_exp_f32_e32 v103, v103
	v_exp_f32_e32 v104, v104
	v_exp_f32_e32 v105, v105
	v_add_u32_e32 v2, s97, v230
	ds_read_b128 v[206:209], v2
	ds_read_b128 v[202:205], v2 offset:4096
	s_waitcnt lgkmcnt(12)
	v_mfma_f32_32x32x16_f16 v[50:65], v[186:189], v[154:157], v[50:65]
	v_exp_f32_e32 v106, v106
	v_exp_f32_e32 v107, v107
	v_exp_f32_e32 v108, v108
	v_exp_f32_e32 v109, v109
	v_add_u32_e32 v2, s97, v231
	ds_read_b128 v[198:201], v2
	ds_read_b128 v[194:197], v2 offset:4096
	s_waitcnt lgkmcnt(12)
	v_mfma_f32_32x32x16_f16 v[66:81], v[182:185], v[154:157], v[66:81]
	v_exp_f32_e32 v110, v110
	v_exp_f32_e32 v111, v111
	v_exp_f32_e32 v112, v112
	v_exp_f32_e32 v113, v113
	v_add_u32_e32 v2, s97, v232
	ds_read_b128 v[190:193], v2
	ds_read_b128 v[186:189], v2 offset:4096
	s_waitcnt lgkmcnt(12)
	v_mfma_f32_32x32x16_f16 v[50:65], v[178:181], v[150:153], v[50:65]
	v_exp_f32_e32 v82, v82
	v_exp_f32_e32 v83, v83
	v_exp_f32_e32 v84, v84
	v_exp_f32_e32 v85, v85
	v_add_u32_e32 v2, s97, v233
	ds_read_b128 v[182:185], v2
	ds_read_b128 v[178:181], v2 offset:4096
	s_waitcnt lgkmcnt(12)
	v_mfma_f32_32x32x16_f16 v[66:81], v[222:225], v[150:153], v[66:81]
	v_exp_f32_e32 v86, v86
	v_exp_f32_e32 v87, v87
	v_exp_f32_e32 v88, v88
	v_exp_f32_e32 v89, v89
	s_waitcnt lgkmcnt(10)
	v_mfma_f32_32x32x16_f16 v[50:65], v[218:221], v[146:149], v[50:65]
	v_exp_f32_e32 v90, v90
	v_exp_f32_e32 v91, v91
	v_exp_f32_e32 v92, v92
	v_exp_f32_e32 v93, v93
	s_waitcnt lgkmcnt(8)
	v_mfma_f32_32x32x16_f16 v[66:81], v[214:217], v[146:149], v[66:81]
	v_exp_f32_e32 v94, v94
	v_exp_f32_e32 v95, v95
	v_exp_f32_e32 v96, v96
	v_exp_f32_e32 v97, v97
	s_setprio 0
	s_waitcnt vmcnt(3)
	v_cvt_pkrtz_f16_f32 v8, v8, v9
	v_cvt_pkrtz_f16_f32 v9, v10, v11
	v_add_u32_e32 v17, s77, v249
	s_waitcnt vmcnt(2)
	v_cvt_pkrtz_f16_f32 v4, v4, v5
	v_cvt_pkrtz_f16_f32 v5, v6, v7
	ds_write2st64_b64 v17, v[8:9], v[4:5] offset1:8
	s_waitcnt vmcnt(1)
	v_cvt_pkrtz_f16_f32 v146, v210, v211
	v_cvt_pkrtz_f16_f32 v147, v212, v213
	s_waitcnt vmcnt(0)
	v_cvt_pkrtz_f16_f32 v16, v12, v13
	v_cvt_pkrtz_f16_f32 v17, v14, v15
	s_andn2_b64 vcc, exec, s[4:5]
	ds_write2st64_b64 v251, v[146:147], v[16:17] offset0:48 offset1:52
	s_add_i32 s4, s77, 0x2000
	s_cmpk_lg_i32 s77, 0x4000
	s_cselect_b32 s97, s4, 0
	s_addk_i32 s99, 0x80
	s_cmp_lt_i32 s98, s82
	s_cbranch_scc0 .Lloads1e_done
	s_add_i32 s4, s98, 1
	s_min_i32 s4, s4, s95
	s_lshl_b32 s5, s4, 18
	s_add_u32 s18, s100, s5
	s_addc_u32 s19, s101, 0
	s_lshl_b32 s5, s98, 18
	s_add_u32 s20, s0, s5
	s_addc_u32 s21, s1, 0
	s_cmp_eq_u32 s4, s95
	s_cbranch_scc1 .Lclamp1e
	global_load_dwordx4 v[8:11], v245, s[18:19]
	global_load_dwordx4 v[4:7], v246, s[18:19]
	global_load_dwordx4 v[130:133], v245, s[20:21]
	global_load_dwordx4 v[12:15], v246, s[20:21]
